# prep_conv gate-row loads hoisted out of the per-token store/load/wait chain
# baseline (speedup 1.0000x reference)
; __device__ __forceinline__ f32x4 bf4(u32x2 v) { return (f32x4){lo_bf(v.x), hi_bf(v.x), lo_bf(v.y), hi_bf(v.y)}; }
; __device__ __forceinline__ void ph_prep_conv(CArgs& a, int l, LAS unsigned char* lds, int bid, int nblk) {
;     ...
;     for (int it = bid + (l == DEPTH - 1 ? 64 : 0); it < 576; it += nblk) {
;         const Chunk c = chunk_of(it);
;         const int tb = c.t0 + tg * 8;
;         const bf16* pb = P + (size_t)(c.row0 + tg * 8) * D_INP;
;         f32x4 x1[10], vv[10], mm[10];
; #pragma unroll
;         for (int r = 0; r < 10; ++r) { const int t = tb + r - 1, tc = min(max(t, c.lo), c.hi - 1); const float ok = (t == tc) ? 1.f : 0.f; const bf16* p = pb + (ptrdiff_t)(tc - tb) * D_INP;
;             x1[r] = ok * bf4(*(const u32x2*)(p + HY0 + 256 + c4)); vv[r] = ok * bf4(*(const u32x2*)(p + HY0 + 512 + c4));
;             mm[r] = ok * bf4(*(const u32x2*)(p + SC0 + 256 + c4)) * bf4(*(const u32x2*)(p + SC0 + 512 + c4)); }
.LBB0_266:
	v_add_u32_e32 v59, s28, v1
	v_add_u32_e32 v56, s11, v1
	v_mov_b64_e32 v[52:53], s[14:15]
	v_mad_i64_i32 v[78:79], s[16:17], v56, s65, v[52:53]
	v_max_i32_e32 v52, s10, v59
	v_min_u32_e32 v60, s9, v52
	v_sub_u32_e32 v52, v60, v59
	v_add_u32_e32 v58, -1, v59
	v_mad_i64_i32 v[52:53], s[16:17], v52, s65, v[78:79]
	v_lshl_add_u64 v[54:55], v[52:53], 0, v[34:35]
	v_max_i32_e32 v52, s10, v58
	v_min_u32_e32 v64, s9, v52
	v_sub_u32_e32 v52, v64, v59
	v_mad_i64_i32 v[52:53], s[16:17], v52, s65, v[78:79]
	v_or_b32_e32 v65, 1, v59
	v_lshl_add_u64 v[62:63], v[52:53], 0, v[34:35]
	v_max_i32_e32 v52, s10, v65
	v_min_u32_e32 v66, s9, v52
	v_sub_u32_e32 v52, v66, v59
	global_load_dwordx2 v[68:69], v[54:55], off offset:2048
	global_load_dwordx2 v[70:71], v[54:55], off offset:2560
	v_mad_i64_i32 v[52:53], s[16:17], v52, s65, v[78:79]
	v_lshl_add_u64 v[86:87], v[52:53], 0, v[34:35]
	global_load_dwordx2 v[82:83], v[62:63], off offset:2048
	global_load_dwordx2 v[84:85], v[62:63], off offset:2560
	global_load_dwordx2 v[88:89], v[86:87], off offset:2048
	global_load_dwordx2 v[90:91], v[86:87], off offset:2560
	v_lshl_add_u64 v[52:53], v[78:79], 0, v[34:35]
	global_load_dwordx2 v[92:93], v[52:53], off offset:1536
	v_or_b32_e32 v61, 2, v59
	v_max_i32_e32 v67, s10, v61
	v_cmp_eq_u32_e32 vcc, v60, v59
	v_min_u32_e32 v73, s9, v67
	v_or_b32_e32 v137, 3, v59
	v_cndmask_b32_e64 v60, 0, 1.0, vcc
	v_cmp_eq_u32_e32 vcc, v58, v64
	v_sub_u32_e32 v64, v73, v59
	v_or_b32_e32 v212, 4, v59
	v_cndmask_b32_e64 v72, 0, 1.0, vcc
	v_cmp_eq_u32_e32 vcc, v65, v66
	v_mad_i64_i32 v[64:65], s[16:17], v64, s65, v[78:79]
	global_load_dwordx2 v[74:75], v[54:55], off offset:512
	global_load_dwordx2 v[66:67], v[54:55], off offset:1024
	v_cndmask_b32_e64 v58, 0, 1.0, vcc
	v_lshl_add_u64 v[98:99], v[64:65], 0, v[34:35]
	global_load_dwordx2 v[80:81], v[62:63], off offset:512
	global_load_dwordx2 v[76:77], v[62:63], off offset:1024
	global_load_dwordx2 v[64:65], v[86:87], off offset:512
	s_nop 0
	global_load_dwordx2 v[62:63], v[86:87], off offset:1024
	v_or_b32_e32 v214, 5, v59
	v_or_b32_e32 v216, 6, v59
	v_or_b32_e32 v211, 7, v59
	v_add_u32_e32 v209, 8, v59
	v_ashrrev_i32_e32 v57, 31, v56
	v_lshlrev_b64 v[56:57], 11, v[56:57]
	v_lshl_add_u64 v[56:57], s[2:3], 0, v[56:57]
	v_lshl_add_u64 v[56:57], v[56:57], 0, v[34:35]
	s_lshl_b32 s78, s30, 1
	s_mov_b32 s29, s79
	s_add_i32 s0, s0, s68
	s_waitcnt vmcnt(0)
	v_lshlrev_b32_e32 v54, 16, v68
	v_and_b32_e32 v55, 0xffff0000, v68
	v_lshlrev_b32_e32 v68, 16, v69
	v_and_b32_e32 v69, 0xffff0000, v69
	v_lshlrev_b32_e32 v86, 16, v70
	v_and_b32_e32 v87, 0xffff0000, v70
	v_lshlrev_b32_e32 v70, 16, v71
	v_and_b32_e32 v71, 0xffff0000, v71
	v_lshlrev_b32_e32 v94, 16, v82
	v_and_b32_e32 v95, 0xffff0000, v82
	v_lshlrev_b32_e32 v82, 16, v83
	v_and_b32_e32 v83, 0xffff0000, v83
	v_pk_mul_f32 v[54:55], v[60:61], v[54:55] op_sel_hi:[0,1]
	v_pk_mul_f32 v[68:69], v[60:61], v[68:69] op_sel_hi:[0,1]
	v_lshlrev_b32_e32 v102, 16, v88
	v_and_b32_e32 v103, 0xffff0000, v88
	v_lshlrev_b32_e32 v88, 16, v89
	v_and_b32_e32 v89, 0xffff0000, v89
	v_lshlrev_b32_e32 v96, 16, v84
	v_and_b32_e32 v97, 0xffff0000, v84
	v_lshlrev_b32_e32 v100, 16, v85
	v_and_b32_e32 v101, 0xffff0000, v85
	v_lshlrev_b32_e32 v104, 16, v90
	v_and_b32_e32 v105, 0xffff0000, v90
	v_lshlrev_b32_e32 v90, 16, v91
	v_and_b32_e32 v91, 0xffff0000, v91
	v_pk_mul_f32 v[82:83], v[72:73], v[82:83] op_sel_hi:[0,1]
	v_pk_mul_f32 v[94:95], v[72:73], v[94:95] op_sel_hi:[0,1]
	v_pk_mul_f32 v[84:85], v[68:69], v[70:71]
	v_pk_mul_f32 v[86:87], v[54:55], v[86:87]
	v_pk_mul_f32 v[54:55], v[58:59], v[102:103] op_sel_hi:[0,1]
	v_pk_mul_f32 v[68:69], v[58:59], v[88:89] op_sel_hi:[0,1]
	v_pk_mul_f32 v[94:95], v[94:95], v[96:97]
	v_pk_mul_f32 v[96:97], v[82:83], v[100:101]
	v_pk_mul_f32 v[68:69], v[68:69], v[90:91]
	v_pk_mul_f32 v[70:71], v[54:55], v[104:105]
	global_load_dwordx2 v[82:83], v[98:99], off offset:512
	global_load_dwordx2 v[54:55], v[98:99], off offset:1024
	global_load_dwordx2 v[90:91], v[98:99], off offset:2048
	global_load_dwordx2 v[88:89], v[98:99], off offset:2560
	v_max_i32_e32 v98, s10, v137
	v_min_u32_e32 v142, s9, v98
	v_sub_u32_e32 v98, v142, v59
	v_mad_i64_i32 v[98:99], s[16:17], v98, s65, v[78:79]
	v_lshl_add_u64 v[98:99], v[98:99], 0, v[34:35]
	global_load_dwordx2 v[120:121], v[98:99], off offset:512
	global_load_dwordx2 v[118:119], v[98:99], off offset:1024
	global_load_dwordx2 v[124:125], v[98:99], off offset:2048
	global_load_dwordx2 v[122:123], v[98:99], off offset:2560
	v_max_i32_e32 v98, s10, v212
	v_min_u32_e32 v213, s9, v98
	v_sub_u32_e32 v98, v213, v59
	v_mad_i64_i32 v[98:99], s[16:17], v98, s65, v[78:79]
	v_lshl_add_u64 v[98:99], v[98:99], 0, v[34:35]
	global_load_dwordx2 v[174:175], v[98:99], off offset:512
	global_load_dwordx2 v[172:173], v[98:99], off offset:1024
	global_load_dwordx2 v[170:171], v[98:99], off offset:2048
	global_load_dwordx2 v[162:163], v[98:99], off offset:2560
	v_max_i32_e32 v98, s10, v214
	v_min_u32_e32 v215, s9, v98
	v_sub_u32_e32 v98, v215, v59
	v_mad_i64_i32 v[98:99], s[16:17], v98, s65, v[78:79]
	v_lshl_add_u64 v[98:99], v[98:99], 0, v[34:35]
	global_load_dwordx2 v[160:161], v[98:99], off offset:512
	global_load_dwordx2 v[158:159], v[98:99], off offset:1024
	global_load_dwordx2 v[128:129], v[98:99], off offset:2048
	global_load_dwordx2 v[126:127], v[98:99], off offset:2560
	v_max_i32_e32 v98, s10, v216
	v_min_u32_e32 v217, s9, v98
	v_sub_u32_e32 v98, v217, v59
	v_mad_i64_i32 v[98:99], s[16:17], v98, s65, v[78:79]
	v_lshl_add_u64 v[98:99], v[98:99], 0, v[34:35]
	global_load_dwordx2 v[156:157], v[98:99], off offset:512
	global_load_dwordx2 v[116:117], v[98:99], off offset:1024
; #define LAS __attribute__((address_space(3)))
; __device__ __forceinline__ unsigned pk2(float lo, float hi) { return f2bf(lo) | (f2bf(hi) << 16); }
; __device__ __forceinline__ f32x4 bf4(u32x2 v) { return (f32x4){lo_bf(v.x), hi_bf(v.x), lo_bf(v.y), hi_bf(v.y)}; }
; __device__ __forceinline__ void ph_prep_conv(CArgs& a, int l, LAS unsigned char* lds, int bid, int nblk) {
;     ...
;         for (int r = 0; r < 10; ++r) { const int t = tb + r - 1, tc = min(max(t, c.lo), c.hi - 1); const float ok = (t == tc) ? 1.f : 0.f; const bf16* p = pb + (ptrdiff_t)(tc - tb) * D_INP;
;             x1[r] = ok * bf4(*(const u32x2*)(p + HY0 + 256 + c4)); vv[r] = ok * bf4(*(const u32x2*)(p + HY0 + 512 + c4));
;             mm[r] = ok * bf4(*(const u32x2*)(p + SC0 + 256 + c4)) * bf4(*(const u32x2*)(p + SC0 + 512 + c4)); }
; #pragma unroll
;         for (int tt = 0; tt < 8; ++tt) {
;             const f32x4 xx = wx[0] * x1[tt] + wx[1] * x1[tt + 1] + wx[2] * x1[tt + 2] + bx, v2 = wv[0] * vv[tt] + wv[1] * vv[tt + 1] + wv[2] * vv[tt + 2] + bv, z = xx * v2;
;             u32x2 zo; zo.x = pk2(z[0], z[1]); zo.y = pk2(z[2], z[3]); *(LAS u32x2*)(zt + (tg * 8 + tt) * 264 + c4) = zo;
;             const f32x4 bg = bf4(*(const u32x2*)(pb + (size_t)tt * D_INP + SC0 + c4));
;             const f32x4 y = bg * (ws3[0] * mm[tt] + ws3[1] * mm[tt + 1] + ws3[2] * mm[tt + 2]);
;             u32x2 yo; yo.x = pk2(y[0], y[1]); yo.y = pk2(y[2], y[3]); *(u32x2*)(YMIX + (size_t)(c.row0 + tg * 8 + tt) * D + 256 + c4) = yo;
;         }
	global_load_dwordx2 v[114:115], v[98:99], off offset:2048
	global_load_dwordx2 v[112:113], v[98:99], off offset:2560
	v_max_i32_e32 v98, s10, v211
	v_min_u32_e32 v218, s9, v98
	v_sub_u32_e32 v98, v218, v59
	v_mad_i64_i32 v[98:99], s[16:17], v98, s65, v[78:79]
	v_lshl_add_u64 v[98:99], v[98:99], 0, v[34:35]
	v_pk_mul_f32 v[132:133], v[14:15], v[86:87]
	global_load_dwordx2 v[110:111], v[98:99], off offset:512
	global_load_dwordx2 v[108:109], v[98:99], off offset:1024
	global_load_dwordx2 v[106:107], v[98:99], off offset:2048
	global_load_dwordx2 v[104:105], v[98:99], off offset:2560
	v_max_i32_e32 v98, s10, v209
	v_pk_fma_f32 v[94:95], v[10:11], v[94:95], v[132:133]
	v_min_u32_e32 v210, s9, v98
	v_lshlrev_b32_e32 v130, 16, v92
	v_and_b32_e32 v131, 0xffff0000, v92
	v_pk_fma_f32 v[94:95], v[36:37], v[70:71], v[94:95]
	v_sub_u32_e32 v59, v210, v59
	v_pk_mul_f32 v[134:135], v[16:17], v[84:85]
	v_pk_mul_f32 v[94:95], v[94:95], v[130:131]
	v_mad_i64_i32 v[78:79], s[10:11], v59, s65, v[78:79]
	v_pk_fma_f32 v[96:97], v[12:13], v[96:97], v[134:135]
	v_bfe_u32 v59, v94, 16, 1
	v_lshlrev_b32_e32 v92, 16, v93
	v_and_b32_e32 v93, 0xffff0000, v93
	v_pk_fma_f32 v[96:97], v[38:39], v[68:69], v[96:97]
	v_add3_u32 v59, v94, v59, s81
	v_bfe_u32 v94, v95, 16, 1
	v_pk_mul_f32 v[92:93], v[96:97], v[92:93]
	v_lshrrev_b32_e32 v59, 16, v59
	v_add3_u32 v94, v95, v94, s81
	v_and_or_b32 v94, v94, s80, v59
	v_bfe_u32 v59, v92, 16, 1
	s_mov_b32 s9, 0x2dc00000
	v_add3_u32 v59, v92, v59, s81
	v_bfe_u32 v92, v93, 16, 1
	v_add_co_u32_e32 v96, vcc, s9, v56
	v_lshrrev_b32_e32 v59, 16, v59
	v_add3_u32 v92, v93, v92, s81
	v_addc_co_u32_e32 v97, vcc, 0, v57, vcc
	s_movk_i32 s9, 0x2000
	v_lshl_add_u64 v[78:79], v[78:79], 0, v[34:35]
	v_and_or_b32 v95, v92, s80, v59
	v_add_co_u32_e32 v92, vcc, s9, v52
	global_load_dwordx2 v[102:103], v[78:79], off offset:512
	global_load_dwordx2 v[100:101], v[78:79], off offset:1024
	global_load_dwordx2 v[98:99], v[78:79], off offset:2048
	s_nop 0
	global_load_dwordx2 v[78:79], v[78:79], off offset:2560
	v_addc_co_u32_e32 v93, vcc, 0, v53, vcc
	global_store_dwordx2 v[96:97], v[94:95], off offset:512
	global_load_dwordx2 v[130:131], v[92:93], off offset:512
	v_add_co_u32_e32 v232, vcc, 0x3000, v52
	s_nop 1
	v_addc_co_u32_e32 v233, vcc, 0, v53, vcc
	global_load_dwordx2 v[220:221], v[232:233], off offset:3584
	v_add_co_u32_e32 v232, vcc, 0x5000, v52
	s_nop 1
	v_addc_co_u32_e32 v233, vcc, 0, v53, vcc
	global_load_dwordx2 v[222:223], v[232:233], off offset:2560
	v_add_co_u32_e32 v232, vcc, 0x7000, v52
	s_nop 1
	v_addc_co_u32_e32 v233, vcc, 0, v53, vcc
	global_load_dwordx2 v[224:225], v[232:233], off offset:1536
	v_add_co_u32_e32 v232, vcc, 0x9000, v52
	s_nop 1
	v_addc_co_u32_e32 v233, vcc, 0, v53, vcc
	global_load_dwordx2 v[226:227], v[232:233], off offset:512
	v_add_co_u32_e32 v232, vcc, 0xa000, v52
	s_nop 1
	v_addc_co_u32_e32 v233, vcc, 0, v53, vcc
	global_load_dwordx2 v[228:229], v[232:233], off offset:3584
	v_add_co_u32_e32 v232, vcc, 0xc000, v52
	s_nop 1
	v_addc_co_u32_e32 v233, vcc, 0, v53, vcc
	global_load_dwordx2 v[230:231], v[232:233], off offset:2560
	v_cmp_eq_u32_e32 vcc, v61, v73
	s_waitcnt vmcnt(27)
	v_lshlrev_b32_e32 v92, 16, v90
	v_and_b32_e32 v93, 0xffff0000, v90
	v_cndmask_b32_e64 v136, 0, 1.0, vcc
	v_lshlrev_b32_e32 v90, 16, v91
	v_and_b32_e32 v91, 0xffff0000, v91
	v_pk_mul_f32 v[90:91], v[136:137], v[90:91] op_sel_hi:[0,1]
	s_waitcnt vmcnt(26)
	v_lshlrev_b32_e32 v132, 16, v88
	v_and_b32_e32 v133, 0xffff0000, v88
	v_lshlrev_b32_e32 v88, 16, v89
	v_and_b32_e32 v89, 0xffff0000, v89
	v_pk_mul_f32 v[94:95], v[136:137], v[92:93] op_sel_hi:[0,1]
	v_pk_mul_f32 v[92:93], v[90:91], v[88:89]
	v_pk_mul_f32 v[94:95], v[94:95], v[132:133]
	v_pk_mul_f32 v[132:133], v[16:17], v[68:69]
	s_movk_i32 s9, 0x3000
	v_pk_fma_f32 v[84:85], v[12:13], v[84:85], v[132:133]
	s_waitcnt vmcnt(0)
	v_lshlrev_b32_e32 v88, 16, v130
	v_and_b32_e32 v89, 0xffff0000, v130
	v_lshlrev_b32_e32 v90, 16, v131
	v_and_b32_e32 v91, 0xffff0000, v131
	v_pk_mul_f32 v[130:131], v[14:15], v[70:71]
	v_pk_fma_f32 v[84:85], v[38:39], v[92:93], v[84:85]
	v_pk_fma_f32 v[86:87], v[10:11], v[86:87], v[130:131]
	v_pk_mul_f32 v[84:85], v[84:85], v[90:91]
	v_pk_fma_f32 v[86:87], v[36:37], v[94:95], v[86:87]
	s_nop 0
	v_pk_mul_f32 v[86:87], v[86:87], v[88:89]
	s_nop 0
	v_bfe_u32 v59, v86, 16, 1
	v_add3_u32 v59, v86, v59, s81
	v_bfe_u32 v61, v87, 16, 1
	v_lshrrev_b32_e32 v59, 16, v59
	v_add3_u32 v61, v87, v61, s81
	v_and_or_b32 v86, v61, s80, v59
	v_bfe_u32 v59, v84, 16, 1
	v_add3_u32 v59, v84, v59, s81
	v_bfe_u32 v61, v85, 16, 1
	v_lshrrev_b32_e32 v59, 16, v59
	v_add3_u32 v61, v85, v61, s81
	v_and_or_b32 v87, v61, s80, v59
	global_store_dwordx2 v[96:97], v[86:87], off offset:2560
	s_nop 0
	v_lshlrev_b32_e32 v86, 16, v80
	v_and_b32_e32 v87, 0xffff0000, v80
	v_lshlrev_b32_e32 v80, 16, v81
	v_and_b32_e32 v81, 0xffff0000, v81
	v_pk_mul_f32 v[176:177], v[72:73], v[80:81] op_sel_hi:[0,1]
	v_lshlrev_b32_e32 v80, 16, v76
	v_and_b32_e32 v81, 0xffff0000, v76
	v_lshlrev_b32_e32 v76, 16, v77
	v_and_b32_e32 v77, 0xffff0000, v77
	v_pk_mul_f32 v[178:179], v[72:73], v[86:87] op_sel_hi:[0,1]
	v_pk_mul_f32 v[152:153], v[72:73], v[76:77] op_sel_hi:[0,1]
	v_pk_mul_f32 v[154:155], v[72:73], v[80:81] op_sel_hi:[0,1]
	v_lshlrev_b32_e32 v72, 16, v74
	v_and_b32_e32 v73, 0xffff0000, v74
	v_lshlrev_b32_e32 v74, 16, v75
	v_and_b32_e32 v75, 0xffff0000, v75
	v_pk_mul_f32 v[148:149], v[60:61], v[72:73] op_sel_hi:[0,1]
	v_lshlrev_b32_e32 v72, 16, v66
	v_and_b32_e32 v73, 0xffff0000, v66
	v_lshlrev_b32_e32 v66, 16, v67
	v_and_b32_e32 v67, 0xffff0000, v67
	v_pk_mul_f32 v[150:151], v[60:61], v[74:75] op_sel_hi:[0,1]
; #define LAS __attribute__((address_space(3)))
; __device__ __forceinline__ unsigned pk2(float lo, float hi) { return f2bf(lo) | (f2bf(hi) << 16); }
; __device__ __forceinline__ f32x4 bf4(u32x2 v) { return (f32x4){lo_bf(v.x), hi_bf(v.x), lo_bf(v.y), hi_bf(v.y)}; }
; __device__ __forceinline__ void ph_prep_conv(CArgs& a, int l, LAS unsigned char* lds, int bid, int nblk) {
;     ...
;         for (int tt = 0; tt < 8; ++tt) {
;             const f32x4 xx = wx[0] * x1[tt] + wx[1] * x1[tt + 1] + wx[2] * x1[tt + 2] + bx, v2 = wv[0] * vv[tt] + wv[1] * vv[tt + 1] + wv[2] * vv[tt + 2] + bv, z = xx * v2;
;             u32x2 zo; zo.x = pk2(z[0], z[1]); zo.y = pk2(z[2], z[3]); *(LAS u32x2*)(zt + (tg * 8 + tt) * 264 + c4) = zo;
;             const f32x4 bg = bf4(*(const u32x2*)(pb + (size_t)tt * D_INP + SC0 + c4));
;             const f32x4 y = bg * (ws3[0] * mm[tt] + ws3[1] * mm[tt + 1] + ws3[2] * mm[tt + 2]);
;             u32x2 yo; yo.x = pk2(y[0], y[1]); yo.y = pk2(y[2], y[3]); *(u32x2*)(YMIX + (size_t)(c.row0 + tg * 8 + tt) * D + 256 + c4) = yo;
;         }
	v_pk_mul_f32 v[144:145], v[60:61], v[72:73] op_sel_hi:[0,1]
	v_pk_mul_f32 v[146:147], v[60:61], v[66:67] op_sel_hi:[0,1]
	v_lshlrev_b32_e32 v60, 16, v64
	v_and_b32_e32 v61, 0xffff0000, v64
	v_lshlrev_b32_e32 v64, 16, v65
	v_and_b32_e32 v65, 0xffff0000, v65
	v_pk_mul_f32 v[138:139], v[58:59], v[60:61] op_sel_hi:[0,1]
	v_lshlrev_b32_e32 v60, 16, v62
	v_and_b32_e32 v61, 0xffff0000, v62
	v_lshlrev_b32_e32 v62, 16, v63
	v_and_b32_e32 v63, 0xffff0000, v63
	v_pk_mul_f32 v[140:141], v[58:59], v[64:65] op_sel_hi:[0,1]
	v_pk_mul_f32 v[130:131], v[58:59], v[60:61] op_sel_hi:[0,1]
	v_pk_mul_f32 v[132:133], v[58:59], v[62:63] op_sel_hi:[0,1]
	v_lshlrev_b32_e32 v58, 16, v82
	v_and_b32_e32 v59, 0xffff0000, v82
	v_cmp_eq_u32_e32 vcc, v137, v142
	v_pk_mul_f32 v[72:73], v[136:137], v[58:59] op_sel_hi:[0,1]
	v_lshlrev_b32_e32 v62, 16, v124
	v_cndmask_b32_e64 v58, 0, 1.0, vcc
	v_and_b32_e32 v63, 0xffff0000, v124
	v_pk_mul_f32 v[62:63], v[58:59], v[62:63] op_sel_hi:[0,1]
	v_lshlrev_b32_e32 v66, 16, v122
	v_and_b32_e32 v67, 0xffff0000, v122
	v_pk_mul_f32 v[182:183], v[62:63], v[66:67]
	v_pk_mul_f32 v[66:67], v[14:15], v[94:95]
	v_lshlrev_b32_e32 v64, 16, v125
	v_and_b32_e32 v65, 0xffff0000, v125
	v_pk_fma_f32 v[66:67], v[10:11], v[70:71], v[66:67]
	v_pk_mul_f32 v[64:65], v[58:59], v[64:65] op_sel_hi:[0,1]
	v_lshlrev_b32_e32 v74, 16, v123
	v_and_b32_e32 v75, 0xffff0000, v123
	v_pk_fma_f32 v[66:67], v[36:37], v[182:183], v[66:67]
	v_pk_mul_f32 v[180:181], v[64:65], v[74:75]
	v_pk_mul_f32 v[74:75], v[16:17], v[92:93]
	s_mov_b32 s9, 0x2dc01000
	v_pk_fma_f32 v[68:69], v[12:13], v[68:69], v[74:75]
	v_lshlrev_b32_e32 v60, 16, v83
	v_pk_fma_f32 v[68:69], v[38:39], v[180:181], v[68:69]
	v_and_b32_e32 v61, 0xffff0000, v83
	v_pk_mul_f32 v[142:143], v[136:137], v[60:61] op_sel_hi:[0,1]
	v_lshlrev_b32_e32 v60, 16, v54
	v_and_b32_e32 v61, 0xffff0000, v54
	v_lshlrev_b32_e32 v54, 16, v55
	v_and_b32_e32 v55, 0xffff0000, v55
	v_pk_mul_f32 v[134:135], v[136:137], v[60:61] op_sel_hi:[0,1]
	v_pk_mul_f32 v[136:137], v[136:137], v[54:55] op_sel_hi:[0,1]
	v_lshlrev_b32_e32 v54, 16, v120
	v_and_b32_e32 v55, 0xffff0000, v120
	v_lshlrev_b32_e32 v60, 16, v121
	v_and_b32_e32 v61, 0xffff0000, v121
	v_lshlrev_b32_e32 v74, 16, v129
	v_and_b32_e32 v75, 0xffff0000, v129
	v_lshlrev_b32_e32 v76, 16, v127
	v_and_b32_e32 v77, 0xffff0000, v127
	v_pk_mul_f32 v[82:83], v[16:17], v[180:181]
	v_lshlrev_b32_e32 v96, 16, v109
	v_lshlrev_b32_e32 v62, 16, v220
	v_and_b32_e32 v63, 0xffff0000, v220
	v_pk_mul_f32 v[62:63], v[66:67], v[62:63]
	v_lshlrev_b32_e32 v64, 16, v221
	v_bfe_u32 v59, v62, 16, 1
	v_and_b32_e32 v65, 0xffff0000, v221
	v_add3_u32 v59, v62, v59, s81
	v_bfe_u32 v62, v63, 16, 1
	v_pk_mul_f32 v[64:65], v[68:69], v[64:65]
	v_lshrrev_b32_e32 v59, 16, v59
	v_add3_u32 v62, v63, v62, s81
	v_and_or_b32 v62, v62, s80, v59
	v_bfe_u32 v59, v64, 16, 1
	v_add3_u32 v59, v64, v59, s81
	v_bfe_u32 v63, v65, 16, 1
	v_lshrrev_b32_e32 v59, 16, v59
	v_add3_u32 v63, v65, v63, s81
	v_add_co_u32_e32 v68, vcc, s9, v56
	v_and_or_b32 v63, v63, s80, v59
	s_nop 0
	v_addc_co_u32_e32 v69, vcc, 0, v57, vcc
	s_movk_i32 s9, 0x5000
	global_store_dwordx2 v[68:69], v[62:63], off offset:512
	v_pk_mul_f32 v[122:123], v[58:59], v[54:55] op_sel_hi:[0,1]
	s_nop 0
	v_pk_mul_f32 v[124:125], v[58:59], v[60:61] op_sel_hi:[0,1]
	v_lshlrev_b32_e32 v54, 16, v118
	v_and_b32_e32 v55, 0xffff0000, v118
	v_lshlrev_b32_e32 v60, 16, v119
	v_and_b32_e32 v61, 0xffff0000, v119
	v_cmp_eq_u32_e32 vcc, v212, v213
	v_pk_mul_f32 v[118:119], v[58:59], v[54:55] op_sel_hi:[0,1]
	v_pk_mul_f32 v[120:121], v[58:59], v[60:61] op_sel_hi:[0,1]
	v_cndmask_b32_e64 v54, 0, 1.0, vcc
	v_lshlrev_b32_e32 v58, 16, v174
	v_and_b32_e32 v59, 0xffff0000, v174
	v_lshlrev_b32_e32 v60, 16, v175
	v_and_b32_e32 v61, 0xffff0000, v175
	v_pk_mul_f32 v[88:89], v[54:55], v[58:59] op_sel_hi:[0,1]
	v_pk_mul_f32 v[90:91], v[54:55], v[60:61] op_sel_hi:[0,1]
	v_lshlrev_b32_e32 v58, 16, v172
	v_and_b32_e32 v59, 0xffff0000, v172
	v_lshlrev_b32_e32 v60, 16, v173
	v_and_b32_e32 v61, 0xffff0000, v173
	v_pk_mul_f32 v[84:85], v[54:55], v[58:59] op_sel_hi:[0,1]
	v_pk_mul_f32 v[86:87], v[54:55], v[60:61] op_sel_hi:[0,1]
	v_lshlrev_b32_e32 v58, 16, v170
	v_and_b32_e32 v59, 0xffff0000, v170
	v_lshlrev_b32_e32 v60, 16, v171
	v_and_b32_e32 v61, 0xffff0000, v171
	v_pk_mul_f32 v[58:59], v[54:55], v[58:59] op_sel_hi:[0,1]
	v_pk_mul_f32 v[54:55], v[54:55], v[60:61] op_sel_hi:[0,1]
	v_lshlrev_b32_e32 v60, 16, v162
	v_and_b32_e32 v61, 0xffff0000, v162
	v_lshlrev_b32_e32 v62, 16, v163
	v_and_b32_e32 v63, 0xffff0000, v163
	v_cmp_eq_u32_e32 vcc, v214, v215
	v_pk_mul_f32 v[162:163], v[54:55], v[62:63]
	v_pk_mul_f32 v[170:171], v[58:59], v[60:61]
	v_cndmask_b32_e64 v54, 0, 1.0, vcc
	v_lshlrev_b32_e32 v58, 16, v160
	v_and_b32_e32 v59, 0xffff0000, v160
	v_lshlrev_b32_e32 v60, 16, v161
	v_and_b32_e32 v61, 0xffff0000, v161
	v_pk_mul_f32 v[64:65], v[54:55], v[58:59] op_sel_hi:[0,1]
	v_lshlrev_b32_e32 v58, 16, v158
	v_and_b32_e32 v59, 0xffff0000, v158
	v_pk_mul_f32 v[66:67], v[54:55], v[60:61] op_sel_hi:[0,1]
	v_lshlrev_b32_e32 v62, 16, v159
	v_and_b32_e32 v63, 0xffff0000, v159
	v_pk_mul_f32 v[60:61], v[54:55], v[58:59] op_sel_hi:[0,1]
	v_lshlrev_b32_e32 v58, 16, v128
	v_and_b32_e32 v59, 0xffff0000, v128
	v_pk_mul_f32 v[62:63], v[54:55], v[62:63] op_sel_hi:[0,1]
	v_pk_mul_f32 v[58:59], v[54:55], v[58:59] op_sel_hi:[0,1]
	v_pk_mul_f32 v[54:55], v[54:55], v[74:75] op_sel_hi:[0,1]
	v_lshlrev_b32_e32 v74, 16, v126
	v_and_b32_e32 v75, 0xffff0000, v126
	v_pk_mul_f32 v[126:127], v[54:55], v[76:77]
	v_pk_mul_f32 v[76:77], v[14:15], v[182:183]
	v_pk_mul_f32 v[128:129], v[58:59], v[74:75]
	v_pk_fma_f32 v[76:77], v[10:11], v[94:95], v[76:77]
; #define LAS __attribute__((address_space(3)))
; __device__ __forceinline__ unsigned pk2(float lo, float hi) { return f2bf(lo) | (f2bf(hi) << 16); }
; __device__ __forceinline__ f32x4 bf4(u32x2 v) { return (f32x4){lo_bf(v.x), hi_bf(v.x), lo_bf(v.y), hi_bf(v.y)}; }
; __device__ __forceinline__ void ph_prep_conv(CArgs& a, int l, LAS unsigned char* lds, int bid, int nblk) {
;     ...
;         for (int tt = 0; tt < 8; ++tt) {
;             const f32x4 xx = wx[0] * x1[tt] + wx[1] * x1[tt + 1] + wx[2] * x1[tt + 2] + bx, v2 = wv[0] * vv[tt] + wv[1] * vv[tt + 1] + wv[2] * vv[tt + 2] + bv, z = xx * v2;
;             u32x2 zo; zo.x = pk2(z[0], z[1]); zo.y = pk2(z[2], z[3]); *(LAS u32x2*)(zt + (tg * 8 + tt) * 264 + c4) = zo;
;             const f32x4 bg = bf4(*(const u32x2*)(pb + (size_t)tt * D_INP + SC0 + c4));
;             const f32x4 y = bg * (ws3[0] * mm[tt] + ws3[1] * mm[tt + 1] + ws3[2] * mm[tt + 2]);
;             u32x2 yo; yo.x = pk2(y[0], y[1]); yo.y = pk2(y[2], y[3]); *(u32x2*)(YMIX + (size_t)(c.row0 + tg * 8 + tt) * D + 256 + c4) = yo;
;         }
	v_pk_fma_f32 v[82:83], v[12:13], v[92:93], v[82:83]
	v_pk_fma_f32 v[76:77], v[36:37], v[170:171], v[76:77]
	v_pk_fma_f32 v[82:83], v[38:39], v[162:163], v[82:83]
	v_cmp_eq_u32_e32 vcc, v216, v217
	s_movk_i32 s9, 0x7000
	v_lshlrev_b32_e32 v54, 16, v156
	v_cndmask_b32_e64 v80, 0, 1.0, vcc
	v_and_b32_e32 v55, 0xffff0000, v156
	v_lshlrev_b32_e32 v58, 16, v157
	v_and_b32_e32 v59, 0xffff0000, v157
	v_pk_mul_f32 v[158:159], v[14:15], v[170:171]
	v_pk_mul_f32 v[160:161], v[16:17], v[162:163]
	v_pk_fma_f32 v[158:159], v[10:11], v[182:183], v[158:159]
	v_pk_fma_f32 v[160:161], v[12:13], v[180:181], v[160:161]
	v_pk_fma_f32 v[158:159], v[36:37], v[128:129], v[158:159]
	v_pk_fma_f32 v[160:161], v[38:39], v[126:127], v[160:161]
	v_pk_mul_f32 v[54:55], v[80:81], v[54:55] op_sel_hi:[0,1]
	v_pk_mul_f32 v[58:59], v[80:81], v[58:59] op_sel_hi:[0,1]
	v_lshlrev_b32_e32 v92, 16, v111
	v_and_b32_e32 v93, 0xffff0000, v111
	v_and_b32_e32 v97, 0xffff0000, v109
	v_lshlrev_b32_e32 v74, 16, v222
	v_and_b32_e32 v75, 0xffff0000, v222
	v_pk_mul_f32 v[74:75], v[76:77], v[74:75]
	v_lshlrev_b32_e32 v70, 16, v223
	v_bfe_u32 v76, v74, 16, 1
	v_and_b32_e32 v71, 0xffff0000, v223
	v_add3_u32 v74, v74, v76, s81
	v_bfe_u32 v76, v75, 16, 1
	v_pk_mul_f32 v[70:71], v[82:83], v[70:71]
	v_lshrrev_b32_e32 v74, 16, v74
	v_add3_u32 v75, v75, v76, s81
	v_and_or_b32 v74, v75, s80, v74
	v_bfe_u32 v75, v70, 16, 1
	v_add3_u32 v70, v70, v75, s81
	v_bfe_u32 v75, v71, 16, 1
	v_lshrrev_b32_e32 v70, 16, v70
	v_add3_u32 v71, v71, v75, s81
	v_and_or_b32 v75, v71, s80, v70
	global_store_dwordx2 v[68:69], v[74:75], off offset:2560
	v_lshlrev_b32_e32 v70, 16, v117
	s_nop 0
	v_lshlrev_b32_e32 v68, 16, v116
	v_and_b32_e32 v69, 0xffff0000, v116
	v_and_b32_e32 v71, 0xffff0000, v117
	v_pk_mul_f32 v[74:75], v[80:81], v[68:69] op_sel_hi:[0,1]
	v_pk_mul_f32 v[76:77], v[80:81], v[70:71] op_sel_hi:[0,1]
	v_lshlrev_b32_e32 v68, 16, v114
	v_and_b32_e32 v69, 0xffff0000, v114
	v_lshlrev_b32_e32 v70, 16, v115
	v_and_b32_e32 v71, 0xffff0000, v115
	v_pk_mul_f32 v[82:83], v[80:81], v[68:69] op_sel_hi:[0,1]
	v_pk_mul_f32 v[68:69], v[80:81], v[70:71] op_sel_hi:[0,1]
	v_lshlrev_b32_e32 v70, 16, v112
	v_and_b32_e32 v71, 0xffff0000, v112
	v_lshlrev_b32_e32 v80, 16, v113
	v_and_b32_e32 v81, 0xffff0000, v113
	v_cmp_eq_u32_e32 vcc, v211, v218
	v_pk_mul_f32 v[68:69], v[68:69], v[80:81]
	v_pk_mul_f32 v[70:71], v[82:83], v[70:71]
	v_cndmask_b32_e64 v80, 0, 1.0, vcc
	v_lshlrev_b32_e32 v82, 16, v110
	v_and_b32_e32 v83, 0xffff0000, v110
	v_cmp_eq_u32_e32 vcc, v209, v210
	s_mov_b32 s9, 0x2dc02000
	v_pk_mul_f32 v[94:95], v[80:81], v[82:83] op_sel_hi:[0,1]
	v_lshlrev_b32_e32 v82, 16, v108
	v_and_b32_e32 v83, 0xffff0000, v108
	v_cndmask_b32_e64 v108, 0, 1.0, vcc
	v_pk_mul_f32 v[110:111], v[80:81], v[92:93] op_sel_hi:[0,1]
	v_pk_mul_f32 v[92:93], v[80:81], v[82:83] op_sel_hi:[0,1]
	v_lshlrev_b32_e32 v82, 16, v106
	v_and_b32_e32 v83, 0xffff0000, v106
	v_lshlrev_b32_e32 v106, 16, v107
	v_and_b32_e32 v107, 0xffff0000, v107
	v_pk_mul_f32 v[96:97], v[80:81], v[96:97] op_sel_hi:[0,1]
	v_pk_mul_f32 v[82:83], v[80:81], v[82:83] op_sel_hi:[0,1]
	v_pk_mul_f32 v[80:81], v[80:81], v[106:107] op_sel_hi:[0,1]
	v_lshlrev_b32_e32 v106, 16, v104
	v_and_b32_e32 v107, 0xffff0000, v104
	v_lshlrev_b32_e32 v104, 16, v105
	v_and_b32_e32 v105, 0xffff0000, v105
	v_pk_mul_f32 v[80:81], v[80:81], v[104:105]
	v_lshlrev_b32_e32 v104, 16, v102
	v_and_b32_e32 v105, 0xffff0000, v102
	v_pk_mul_f32 v[82:83], v[82:83], v[106:107]
	v_lshlrev_b32_e32 v106, 16, v103
	v_and_b32_e32 v107, 0xffff0000, v103
	v_pk_mul_f32 v[102:103], v[108:109], v[104:105] op_sel_hi:[0,1]
	v_lshlrev_b32_e32 v104, 16, v100
	v_and_b32_e32 v105, 0xffff0000, v100
	v_lshlrev_b32_e32 v112, 16, v101
	v_and_b32_e32 v113, 0xffff0000, v101
	v_pk_mul_f32 v[100:101], v[108:109], v[104:105] op_sel_hi:[0,1]
	v_pk_mul_f32 v[104:105], v[108:109], v[112:113] op_sel_hi:[0,1]
	v_lshlrev_b32_e32 v112, 16, v98
	v_and_b32_e32 v113, 0xffff0000, v98
	v_lshlrev_b32_e32 v98, 16, v99
	v_and_b32_e32 v99, 0xffff0000, v99
	v_pk_mul_f32 v[106:107], v[108:109], v[106:107] op_sel_hi:[0,1]
	v_pk_mul_f32 v[112:113], v[108:109], v[112:113] op_sel_hi:[0,1]
	v_pk_mul_f32 v[98:99], v[108:109], v[98:99] op_sel_hi:[0,1]
	v_lshlrev_b32_e32 v108, 16, v78
	v_and_b32_e32 v109, 0xffff0000, v78
	v_lshlrev_b32_e32 v78, 16, v79
	v_and_b32_e32 v79, 0xffff0000, v79
	v_pk_mul_f32 v[78:79], v[98:99], v[78:79]
	v_pk_mul_f32 v[98:99], v[112:113], v[108:109]
	v_pk_mul_f32 v[112:113], v[26:27], v[148:149]
	v_pk_mul_f32 v[108:109], v[28:29], v[150:151]
	v_pk_fma_f32 v[112:113], v[2:3], v[178:179], v[112:113]
	v_pk_mul_f32 v[114:115], v[20:21], v[146:147]
	v_pk_fma_f32 v[108:109], v[4:5], v[176:177], v[108:109]
	v_pk_fma_f32 v[112:113], v[22:23], v[138:139], v[112:113]
	v_pk_fma_f32 v[114:115], v[8:9], v[152:153], v[114:115]
	v_pk_fma_f32 v[108:109], v[24:25], v[140:141], v[108:109]
	v_pk_add_f32 v[112:113], v[40:41], v[112:113]
	v_pk_fma_f32 v[114:115], v[32:33], v[132:133], v[114:115]
	v_pk_add_f32 v[108:109], v[42:43], v[108:109]
	v_pk_add_f32 v[114:115], v[46:47], v[114:115]
	v_lshlrev_b32_e32 v116, 16, v224
	v_and_b32_e32 v117, 0xffff0000, v224
	v_pk_mul_f32 v[116:117], v[158:159], v[116:117]
	v_lshlrev_b32_e32 v156, 16, v225
	v_bfe_u32 v158, v116, 16, 1
	v_and_b32_e32 v157, 0xffff0000, v225
	v_add3_u32 v116, v116, v158, s81
	v_bfe_u32 v158, v117, 16, 1
	v_pk_mul_f32 v[156:157], v[160:161], v[156:157]
	v_lshrrev_b32_e32 v116, 16, v116
	v_add3_u32 v117, v117, v158, s81
	v_and_or_b32 v116, v117, s80, v116
	v_bfe_u32 v117, v156, 16, 1
	v_add3_u32 v117, v156, v117, s81
	v_bfe_u32 v156, v157, 16, 1
	v_lshrrev_b32_e32 v117, 16, v117
; #define LAS __attribute__((address_space(3)))
; __device__ __forceinline__ unsigned pk2(float lo, float hi) { return f2bf(lo) | (f2bf(hi) << 16); }
; __device__ __forceinline__ f32x4 bf4(u32x2 v) { return (f32x4){lo_bf(v.x), hi_bf(v.x), lo_bf(v.y), hi_bf(v.y)}; }
; __device__ __forceinline__ void ph_prep_conv(CArgs& a, int l, LAS unsigned char* lds, int bid, int nblk) {
;     ...
;         for (int tt = 0; tt < 8; ++tt) {
;             const f32x4 xx = wx[0] * x1[tt] + wx[1] * x1[tt + 1] + wx[2] * x1[tt + 2] + bx, v2 = wv[0] * vv[tt] + wv[1] * vv[tt + 1] + wv[2] * vv[tt + 2] + bv, z = xx * v2;
;             u32x2 zo; zo.x = pk2(z[0], z[1]); zo.y = pk2(z[2], z[3]); *(LAS u32x2*)(zt + (tg * 8 + tt) * 264 + c4) = zo;
;             const f32x4 bg = bf4(*(const u32x2*)(pb + (size_t)tt * D_INP + SC0 + c4));
;             const f32x4 y = bg * (ws3[0] * mm[tt] + ws3[1] * mm[tt + 1] + ws3[2] * mm[tt + 2]);
;             u32x2 yo; yo.x = pk2(y[0], y[1]); yo.y = pk2(y[2], y[3]); *(u32x2*)(YMIX + (size_t)(c.row0 + tg * 8 + tt) * D + 256 + c4) = yo;
;         }
	v_add3_u32 v156, v157, v156, s81
	v_and_or_b32 v117, v156, s80, v117
	v_add_co_u32_e32 v156, vcc, s9, v56
	s_mov_b32 s9, 0x9000
	s_nop 0
	v_addc_co_u32_e32 v157, vcc, 0, v57, vcc
	global_store_dwordx2 v[156:157], v[116:117], off offset:512
	v_pk_mul_f32 v[158:159], v[18:19], v[144:145]
	s_nop 0
	v_pk_fma_f32 v[154:155], v[6:7], v[154:155], v[158:159]
	v_pk_mul_f32 v[108:109], v[108:109], v[114:115]
	v_pk_fma_f32 v[152:153], v[30:31], v[130:131], v[154:155]
	s_mov_b32 s9, 0xa000
	v_pk_add_f32 v[152:153], v[44:45], v[152:153]
	s_nop 0
	v_pk_mul_f32 v[112:113], v[112:113], v[152:153]
	s_nop 0
	v_bfe_u32 v114, v112, 16, 1
	v_add3_u32 v112, v112, v114, s81
	v_bfe_u32 v114, v113, 16, 1
	v_lshrrev_b32_e32 v112, 16, v112
	v_add3_u32 v113, v113, v114, s81
	v_and_or_b32 v112, v113, s80, v112
	v_bfe_u32 v113, v108, 16, 1
	v_add3_u32 v108, v108, v113, s81
	v_bfe_u32 v113, v109, 16, 1
	v_lshrrev_b32_e32 v108, 16, v108
	v_add3_u32 v109, v109, v113, s81
	v_and_or_b32 v113, v109, s80, v108
	v_pk_mul_f32 v[108:109], v[28:29], v[140:141]
	v_pk_mul_f32 v[114:115], v[26:27], v[138:139]
	v_pk_fma_f32 v[108:109], v[4:5], v[150:151], v[108:109]
	v_pk_mul_f32 v[150:151], v[18:19], v[130:131]
	v_pk_fma_f32 v[114:115], v[2:3], v[148:149], v[114:115]
	v_pk_fma_f32 v[144:145], v[6:7], v[144:145], v[150:151]
	v_pk_fma_f32 v[114:115], v[22:23], v[72:73], v[114:115]
	v_pk_fma_f32 v[144:145], v[30:31], v[134:135], v[144:145]
	v_pk_add_f32 v[114:115], v[40:41], v[114:115]
	v_pk_mul_f32 v[148:149], v[20:21], v[132:133]
	v_pk_add_f32 v[144:145], v[44:45], v[144:145]
	v_pk_fma_f32 v[146:147], v[8:9], v[146:147], v[148:149]
	v_pk_mul_f32 v[114:115], v[114:115], v[144:145]
	v_pk_fma_f32 v[108:109], v[24:25], v[142:143], v[108:109]
	v_pk_fma_f32 v[146:147], v[32:33], v[136:137], v[146:147]
	v_bfe_u32 v144, v114, 16, 1
	v_pk_add_f32 v[108:109], v[42:43], v[108:109]
	v_pk_add_f32 v[146:147], v[46:47], v[146:147]
	v_add3_u32 v114, v114, v144, s81
	v_bfe_u32 v144, v115, 16, 1
	v_pk_mul_f32 v[108:109], v[108:109], v[146:147]
	v_lshrrev_b32_e32 v114, 16, v114
	v_add3_u32 v115, v115, v144, s81
	v_and_or_b32 v114, v115, s80, v114
	v_bfe_u32 v115, v108, 16, 1
	v_add3_u32 v108, v108, v115, s81
	v_bfe_u32 v115, v109, 16, 1
	v_lshrrev_b32_e32 v108, 16, v108
	v_add3_u32 v109, v109, v115, s81
	v_and_or_b32 v115, v109, s80, v108
	ds_write2_b64 v185, v[112:113], v[114:115] offset1:66
	v_pk_mul_f32 v[112:113], v[26:27], v[72:73]
	v_pk_mul_f32 v[108:109], v[28:29], v[142:143]
	v_pk_fma_f32 v[112:113], v[2:3], v[138:139], v[112:113]
	v_pk_mul_f32 v[138:139], v[18:19], v[134:135]
	v_pk_mul_f32 v[114:115], v[20:21], v[136:137]
	v_pk_fma_f32 v[130:131], v[6:7], v[130:131], v[138:139]
	v_pk_fma_f32 v[108:109], v[4:5], v[140:141], v[108:109]
	v_pk_fma_f32 v[112:113], v[22:23], v[122:123], v[112:113]
	v_pk_fma_f32 v[114:115], v[8:9], v[132:133], v[114:115]
	v_pk_fma_f32 v[130:131], v[30:31], v[118:119], v[130:131]
	v_pk_fma_f32 v[108:109], v[24:25], v[124:125], v[108:109]
	v_pk_add_f32 v[112:113], v[40:41], v[112:113]
	v_pk_fma_f32 v[114:115], v[32:33], v[120:121], v[114:115]
	v_pk_add_f32 v[130:131], v[44:45], v[130:131]
	v_pk_add_f32 v[108:109], v[42:43], v[108:109]
	v_pk_add_f32 v[114:115], v[46:47], v[114:115]
	v_pk_mul_f32 v[112:113], v[112:113], v[130:131]
	v_pk_mul_f32 v[108:109], v[108:109], v[114:115]
	v_bfe_u32 v114, v112, 16, 1
	v_pk_mul_f32 v[130:131], v[14:15], v[128:129]
	v_add3_u32 v112, v112, v114, s81
	v_bfe_u32 v114, v113, 16, 1
	v_pk_fma_f32 v[130:131], v[10:11], v[170:171], v[130:131]
	v_lshrrev_b32_e32 v112, 16, v112
	v_add3_u32 v113, v113, v114, s81
	v_pk_fma_f32 v[130:131], v[36:37], v[70:71], v[130:131]
	v_and_or_b32 v112, v113, s80, v112
	v_bfe_u32 v113, v108, 16, 1
	v_lshlrev_b32_e32 v114, 16, v226
	v_and_b32_e32 v115, 0xffff0000, v226
	v_pk_mul_f32 v[132:133], v[16:17], v[126:127]
	v_pk_mul_f32 v[114:115], v[130:131], v[114:115]
	v_add3_u32 v108, v108, v113, s81
	v_pk_fma_f32 v[132:133], v[12:13], v[162:163], v[132:133]
	v_bfe_u32 v113, v114, 16, 1
	v_lshlrev_b32_e32 v116, 16, v227
	v_and_b32_e32 v117, 0xffff0000, v227
	v_pk_fma_f32 v[132:133], v[38:39], v[68:69], v[132:133]
	v_add3_u32 v113, v114, v113, s81
	v_bfe_u32 v114, v115, 16, 1
	v_pk_mul_f32 v[116:117], v[132:133], v[116:117]
	v_lshrrev_b32_e32 v113, 16, v113
	v_add3_u32 v114, v115, v114, s81
	v_and_or_b32 v114, v114, s80, v113
	v_bfe_u32 v113, v116, 16, 1
	v_add3_u32 v113, v116, v113, s81
	v_bfe_u32 v115, v117, 16, 1
	v_lshrrev_b32_e32 v113, 16, v113
	v_add3_u32 v115, v117, v115, s81
	v_and_or_b32 v115, v115, s80, v113
	global_store_dwordx2 v[156:157], v[114:115], off offset:2560
	v_bfe_u32 v113, v109, 16, 1
	s_nop 0
	v_lshrrev_b32_e32 v108, 16, v108
	v_add3_u32 v109, v109, v113, s81
	v_pk_mul_f32 v[116:117], v[26:27], v[122:123]
	v_pk_mul_f32 v[130:131], v[18:19], v[118:119]
	v_and_or_b32 v113, v109, s80, v108
	v_pk_mul_f32 v[108:109], v[28:29], v[124:125]
	v_pk_fma_f32 v[72:73], v[2:3], v[72:73], v[116:117]
	v_pk_mul_f32 v[116:117], v[20:21], v[120:121]
	v_pk_fma_f32 v[130:131], v[6:7], v[134:135], v[130:131]
	v_pk_fma_f32 v[108:109], v[4:5], v[142:143], v[108:109]
	v_pk_fma_f32 v[72:73], v[22:23], v[88:89], v[72:73]
	v_pk_fma_f32 v[116:117], v[8:9], v[136:137], v[116:117]
	v_pk_fma_f32 v[130:131], v[30:31], v[84:85], v[130:131]
	v_pk_fma_f32 v[108:109], v[24:25], v[90:91], v[108:109]
	v_pk_add_f32 v[72:73], v[40:41], v[72:73]
	v_pk_fma_f32 v[116:117], v[32:33], v[86:87], v[116:117]
	v_pk_add_f32 v[130:131], v[44:45], v[130:131]
	v_pk_add_f32 v[108:109], v[42:43], v[108:109]
	v_pk_add_f32 v[116:117], v[46:47], v[116:117]
	v_pk_mul_f32 v[72:73], v[72:73], v[130:131]
	v_pk_mul_f32 v[108:109], v[108:109], v[116:117]
; #define LAS __attribute__((address_space(3)))
; __device__ __forceinline__ unsigned pk2(float lo, float hi) { return f2bf(lo) | (f2bf(hi) << 16); }
; __device__ __forceinline__ f32x4 bf4(u32x2 v) { return (f32x4){lo_bf(v.x), hi_bf(v.x), lo_bf(v.y), hi_bf(v.y)}; }
; __device__ __forceinline__ void ph_prep_conv(CArgs& a, int l, LAS unsigned char* lds, int bid, int nblk) {
;     ...
;         for (int tt = 0; tt < 8; ++tt) {
;             const f32x4 xx = wx[0] * x1[tt] + wx[1] * x1[tt + 1] + wx[2] * x1[tt + 2] + bx, v2 = wv[0] * vv[tt] + wv[1] * vv[tt + 1] + wv[2] * vv[tt + 2] + bv, z = xx * v2;
;             u32x2 zo; zo.x = pk2(z[0], z[1]); zo.y = pk2(z[2], z[3]); *(LAS u32x2*)(zt + (tg * 8 + tt) * 264 + c4) = zo;
;             const f32x4 bg = bf4(*(const u32x2*)(pb + (size_t)tt * D_INP + SC0 + c4));
;             const f32x4 y = bg * (ws3[0] * mm[tt] + ws3[1] * mm[tt + 1] + ws3[2] * mm[tt + 2]);
;             u32x2 yo; yo.x = pk2(y[0], y[1]); yo.y = pk2(y[2], y[3]); *(u32x2*)(YMIX + (size_t)(c.row0 + tg * 8 + tt) * D + 256 + c4) = yo;
;         }
	v_bfe_u32 v116, v72, 16, 1
	v_add3_u32 v72, v72, v116, s81
	v_bfe_u32 v116, v73, 16, 1
	v_lshrrev_b32_e32 v72, 16, v72
	v_add3_u32 v73, v73, v116, s81
	v_and_or_b32 v72, v73, s80, v72
	v_bfe_u32 v73, v108, 16, 1
	v_add3_u32 v73, v108, v73, s81
	v_bfe_u32 v108, v109, 16, 1
	v_lshrrev_b32_e32 v73, 16, v73
	v_add3_u32 v108, v109, v108, s81
	v_and_or_b32 v73, v108, s80, v73
	v_pk_mul_f32 v[108:109], v[26:27], v[88:89]
	v_pk_mul_f32 v[116:117], v[18:19], v[84:85]
	ds_write2_b64 v185, v[112:113], v[72:73] offset0:132 offset1:198
	v_pk_mul_f32 v[72:73], v[28:29], v[90:91]
	v_pk_fma_f32 v[108:109], v[2:3], v[122:123], v[108:109]
	v_pk_mul_f32 v[112:113], v[20:21], v[86:87]
	v_pk_fma_f32 v[116:117], v[6:7], v[118:119], v[116:117]
	v_pk_fma_f32 v[72:73], v[4:5], v[124:125], v[72:73]
	v_pk_fma_f32 v[108:109], v[22:23], v[64:65], v[108:109]
	v_pk_fma_f32 v[112:113], v[8:9], v[120:121], v[112:113]
	v_pk_fma_f32 v[116:117], v[30:31], v[60:61], v[116:117]
	v_pk_fma_f32 v[72:73], v[24:25], v[66:67], v[72:73]
	v_pk_add_f32 v[108:109], v[40:41], v[108:109]
	v_pk_fma_f32 v[112:113], v[32:33], v[62:63], v[112:113]
	v_pk_add_f32 v[116:117], v[44:45], v[116:117]
	v_pk_add_f32 v[72:73], v[42:43], v[72:73]
	v_pk_add_f32 v[112:113], v[46:47], v[112:113]
	v_pk_mul_f32 v[108:109], v[108:109], v[116:117]
	v_pk_mul_f32 v[72:73], v[72:73], v[112:113]
	v_bfe_u32 v112, v108, 16, 1
	v_add3_u32 v108, v108, v112, s81
	v_bfe_u32 v112, v109, 16, 1
	v_lshrrev_b32_e32 v108, 16, v108
	v_add3_u32 v109, v109, v112, s81
	v_and_or_b32 v108, v109, s80, v108
	v_bfe_u32 v109, v72, 16, 1
	v_add3_u32 v72, v72, v109, s81
	v_bfe_u32 v109, v73, 16, 1
	v_lshrrev_b32_e32 v72, 16, v72
	v_add3_u32 v73, v73, v109, s81
	v_and_or_b32 v109, v73, s80, v72
	v_pk_mul_f32 v[72:73], v[28:29], v[66:67]
	v_pk_mul_f32 v[112:113], v[26:27], v[64:65]
	v_pk_fma_f32 v[72:73], v[4:5], v[90:91], v[72:73]
	v_pk_fma_f32 v[88:89], v[2:3], v[88:89], v[112:113]
	v_pk_mul_f32 v[90:91], v[20:21], v[62:63]
	v_pk_mul_f32 v[112:113], v[18:19], v[60:61]
	v_pk_fma_f32 v[86:87], v[8:9], v[86:87], v[90:91]
	v_pk_fma_f32 v[84:85], v[6:7], v[84:85], v[112:113]
	v_pk_mul_f32 v[116:117], v[16:17], v[68:69]
	s_mov_b32 s9, 0x2dc03000
	v_pk_fma_f32 v[116:117], v[12:13], v[126:127], v[116:117]
	v_add_co_u32_e32 v56, vcc, s9, v56
	v_pk_fma_f32 v[116:117], v[38:39], v[80:81], v[116:117]
	s_nop 0
	v_addc_co_u32_e32 v57, vcc, 0, v57, vcc
	v_lshlrev_b32_e32 v90, 16, v228
	v_and_b32_e32 v91, 0xffff0000, v228
	v_lshlrev_b32_e32 v112, 16, v229
	v_and_b32_e32 v113, 0xffff0000, v229
	v_pk_mul_f32 v[114:115], v[14:15], v[70:71]
	v_pk_mul_f32 v[112:113], v[116:117], v[112:113]
	v_pk_fma_f32 v[114:115], v[10:11], v[128:129], v[114:115]
	s_mov_b32 s9, 0xc000
	v_pk_fma_f32 v[114:115], v[36:37], v[82:83], v[114:115]
	v_pk_mul_f32 v[90:91], v[114:115], v[90:91]
	s_nop 0
	v_bfe_u32 v114, v90, 16, 1
	v_add3_u32 v90, v90, v114, s81
	v_bfe_u32 v114, v91, 16, 1
	v_lshrrev_b32_e32 v90, 16, v90
	v_add3_u32 v91, v91, v114, s81
	v_and_or_b32 v90, v91, s80, v90
	v_bfe_u32 v91, v112, 16, 1
	v_add3_u32 v91, v112, v91, s81
	v_bfe_u32 v112, v113, 16, 1
	v_lshrrev_b32_e32 v91, 16, v91
	v_add3_u32 v112, v113, v112, s81
	v_and_or_b32 v91, v112, s80, v91
	global_store_dwordx2 v[56:57], v[90:91], off offset:512
	v_pk_fma_f32 v[88:89], v[22:23], v[54:55], v[88:89]
	v_pk_fma_f32 v[84:85], v[30:31], v[74:75], v[84:85]
	v_pk_fma_f32 v[72:73], v[24:25], v[58:59], v[72:73]
	v_pk_add_f32 v[88:89], v[40:41], v[88:89]
	v_pk_fma_f32 v[86:87], v[32:33], v[76:77], v[86:87]
	v_pk_add_f32 v[84:85], v[44:45], v[84:85]
	v_pk_add_f32 v[72:73], v[42:43], v[72:73]
	v_pk_add_f32 v[86:87], v[46:47], v[86:87]
	v_pk_mul_f32 v[84:85], v[88:89], v[84:85]
	v_pk_mul_f32 v[72:73], v[72:73], v[86:87]
	v_bfe_u32 v86, v84, 16, 1
	v_add3_u32 v84, v84, v86, s81
	v_bfe_u32 v86, v85, 16, 1
	v_lshrrev_b32_e32 v84, 16, v84
	v_add3_u32 v85, v85, v86, s81
	v_and_or_b32 v84, v85, s80, v84
	v_bfe_u32 v85, v72, 16, 1
	v_add3_u32 v72, v72, v85, s81
	v_bfe_u32 v85, v73, 16, 1
	v_lshrrev_b32_e32 v72, 16, v72
	v_add3_u32 v73, v73, v85, s81
	v_and_or_b32 v85, v73, s80, v72
	v_add_u32_e32 v72, 0x800, v185
	ds_write2_b64 v72, v[108:109], v[84:85] offset0:8 offset1:74
	v_pk_mul_f32 v[84:85], v[26:27], v[54:55]
	v_pk_mul_f32 v[72:73], v[28:29], v[58:59]
	v_pk_fma_f32 v[64:65], v[2:3], v[64:65], v[84:85]
	v_pk_mul_f32 v[84:85], v[18:19], v[74:75]
	v_pk_fma_f32 v[64:65], v[22:23], v[94:95], v[64:65]
	v_pk_fma_f32 v[60:61], v[6:7], v[60:61], v[84:85]
	v_pk_fma_f32 v[66:67], v[4:5], v[66:67], v[72:73]
	v_pk_fma_f32 v[60:61], v[30:31], v[92:93], v[60:61]
	v_pk_add_f32 v[64:65], v[40:41], v[64:65]
	v_pk_mul_f32 v[72:73], v[20:21], v[76:77]
	v_pk_add_f32 v[60:61], v[44:45], v[60:61]
	v_pk_fma_f32 v[62:63], v[8:9], v[62:63], v[72:73]
	v_pk_mul_f32 v[60:61], v[64:65], v[60:61]
	v_pk_fma_f32 v[66:67], v[24:25], v[110:111], v[66:67]
	v_pk_fma_f32 v[62:63], v[32:33], v[96:97], v[62:63]
	v_bfe_u32 v64, v60, 16, 1
	v_pk_add_f32 v[66:67], v[42:43], v[66:67]
	v_pk_add_f32 v[62:63], v[46:47], v[62:63]
; #define LAS __attribute__((address_space(3)))
; __device__ __forceinline__ unsigned pk2(float lo, float hi) { return f2bf(lo) | (f2bf(hi) << 16); }
; __device__ __forceinline__ f32x4 bf4(u32x2 v) { return (f32x4){lo_bf(v.x), hi_bf(v.x), lo_bf(v.y), hi_bf(v.y)}; }
; __device__ __forceinline__ void ph_prep_conv(CArgs& a, int l, LAS unsigned char* lds, int bid, int nblk) {
;     ...
;         for (int tt = 0; tt < 8; ++tt) {
;             const f32x4 xx = wx[0] * x1[tt] + wx[1] * x1[tt + 1] + wx[2] * x1[tt + 2] + bx, v2 = wv[0] * vv[tt] + wv[1] * vv[tt + 1] + wv[2] * vv[tt + 2] + bv, z = xx * v2;
;             u32x2 zo; zo.x = pk2(z[0], z[1]); zo.y = pk2(z[2], z[3]); *(LAS u32x2*)(zt + (tg * 8 + tt) * 264 + c4) = zo;
;             const f32x4 bg = bf4(*(const u32x2*)(pb + (size_t)tt * D_INP + SC0 + c4));
;             const f32x4 y = bg * (ws3[0] * mm[tt] + ws3[1] * mm[tt + 1] + ws3[2] * mm[tt + 2]);
;             u32x2 yo; yo.x = pk2(y[0], y[1]); yo.y = pk2(y[2], y[3]); *(u32x2*)(YMIX + (size_t)(c.row0 + tg * 8 + tt) * D + 256 + c4) = yo;
;         }
;         __syncthreads();
;         { const int ch = tid & 255, g0 = (tid >> 8) * 4;
;           const int soff = c.L == CTXL ? 0 : CTXL;
; #pragma unroll
;           for (int g = 0; g < 4; ++g) { const int t8 = (g0 + g) * 8; unsigned short e[8];
; #pragma unroll
;               for (int j = 0; j < 8; ++j) e[j] = zt[(t8 + j) * 264 + ch];
;               u32x4 o; o.x = e[0] | ((unsigned)e[1] << 16); o.y = e[2] | ((unsigned)e[3] << 16); o.z = e[4] | ((unsigned)e[5] << 16); o.w = e[6] | ((unsigned)e[7] << 16);
;               *(u32x4*)(ZT + ((size_t)(ch * 16 + c.b)) * 2304 + soff + c.t0 + t8) = o; } }
;         __syncthreads();
	v_add3_u32 v60, v60, v64, s81
	v_bfe_u32 v64, v61, 16, 1
	v_pk_mul_f32 v[62:63], v[66:67], v[62:63]
	v_lshrrev_b32_e32 v60, 16, v60
	v_add3_u32 v61, v61, v64, s81
	v_and_or_b32 v60, v61, s80, v60
	v_bfe_u32 v61, v62, 16, 1
	v_add3_u32 v61, v62, v61, s81
	v_bfe_u32 v62, v63, 16, 1
	v_lshrrev_b32_e32 v61, 16, v61
	v_add3_u32 v62, v63, v62, s81
	v_and_or_b32 v61, v62, s80, v61
	v_pk_mul_f32 v[62:63], v[26:27], v[94:95]
	ds_write_b64 v185, v[60:61] offset:3168
	v_pk_mul_f32 v[60:61], v[28:29], v[110:111]
	v_pk_fma_f32 v[54:55], v[2:3], v[54:55], v[62:63]
	v_pk_mul_f32 v[62:63], v[18:19], v[92:93]
	v_pk_fma_f32 v[58:59], v[4:5], v[58:59], v[60:61]
	v_pk_mul_f32 v[60:61], v[20:21], v[96:97]
	v_pk_fma_f32 v[62:63], v[6:7], v[74:75], v[62:63]
	v_pk_fma_f32 v[54:55], v[22:23], v[102:103], v[54:55]
	v_pk_fma_f32 v[60:61], v[8:9], v[76:77], v[60:61]
	v_pk_fma_f32 v[62:63], v[30:31], v[100:101], v[62:63]
	v_pk_fma_f32 v[58:59], v[24:25], v[106:107], v[58:59]
	v_pk_add_f32 v[54:55], v[40:41], v[54:55]
	v_pk_fma_f32 v[60:61], v[32:33], v[104:105], v[60:61]
	v_pk_add_f32 v[62:63], v[44:45], v[62:63]
	v_pk_add_f32 v[58:59], v[42:43], v[58:59]
	v_pk_add_f32 v[60:61], v[46:47], v[60:61]
	v_pk_mul_f32 v[54:55], v[54:55], v[62:63]
	v_pk_mul_f32 v[58:59], v[58:59], v[60:61]
	v_bfe_u32 v60, v54, 16, 1
	v_add3_u32 v54, v54, v60, s81
	v_bfe_u32 v60, v55, 16, 1
	v_lshrrev_b32_e32 v54, 16, v54
	v_add3_u32 v55, v55, v60, s81
	v_and_or_b32 v54, v55, s80, v54
	v_bfe_u32 v55, v58, 16, 1
	v_add3_u32 v55, v58, v55, s81
	v_bfe_u32 v58, v59, 16, 1
	v_lshrrev_b32_e32 v55, 16, v55
	v_add3_u32 v58, v59, v58, s81
	v_and_or_b32 v55, v58, s80, v55
	v_pk_mul_f32 v[58:59], v[14:15], v[82:83]
	ds_write_b64 v186, v[54:55]
	v_pk_fma_f32 v[58:59], v[10:11], v[70:71], v[58:59]
	v_lshlrev_b32_e32 v54, 16, v230
	v_and_b32_e32 v55, 0xffff0000, v230
	v_pk_fma_f32 v[58:59], v[36:37], v[98:99], v[58:59]
	v_pk_mul_f32 v[60:61], v[16:17], v[80:81]
	v_pk_mul_f32 v[54:55], v[58:59], v[54:55]
	v_pk_fma_f32 v[60:61], v[12:13], v[68:69], v[60:61]
	v_bfe_u32 v58, v54, 16, 1
	v_lshlrev_b32_e32 v52, 16, v231
	v_and_b32_e32 v53, 0xffff0000, v231
	v_pk_fma_f32 v[60:61], v[38:39], v[78:79], v[60:61]
	v_add3_u32 v54, v54, v58, s81
	v_bfe_u32 v58, v55, 16, 1
	v_pk_mul_f32 v[52:53], v[60:61], v[52:53]
	v_lshrrev_b32_e32 v54, 16, v54
	v_add3_u32 v55, v55, v58, s81
	v_and_or_b32 v54, v55, s80, v54
	v_bfe_u32 v55, v52, 16, 1
	v_add3_u32 v52, v52, v55, s81
	v_bfe_u32 v55, v53, 16, 1
	v_lshrrev_b32_e32 v52, 16, v52
	v_add3_u32 v53, v53, v55, s81
	v_and_or_b32 v55, v53, s80, v52
	global_store_dwordx2 v[56:57], v[54:55], off offset:2560
	v_add_u32_e32 v54, s8, v184
	v_mov_b64_e32 v[52:53], s[26:27]
	s_movk_i32 s8, 0x1200
	s_waitcnt lgkmcnt(0)
	s_barrier
	v_mad_i64_i32 v[52:53], s[8:9], v54, s8, v[52:53]
	ds_read_u16 v58, v187
	ds_read_u16 v59, v187 offset:528
	ds_read_u16 v60, v187 offset:1056
	ds_read_u16 v61, v187 offset:1584
	ds_read_u16 v54, v187 offset:2112
	ds_read_u16 v62, v187 offset:2640
	ds_read_u16 v55, v187 offset:3168
	ds_read_u16 v63, v187 offset:3696
	v_lshl_add_u64 v[52:53], v[52:53], 0, s[78:79]
	v_lshl_add_u64 v[56:57], s[28:29], 1, v[52:53]
	s_mov_b32 s8, 0x5040100
	s_waitcnt lgkmcnt(2)
	v_perm_b32 v54, v62, v54, s8
	s_waitcnt lgkmcnt(0)
	v_perm_b32 v55, v63, v55, s8
	v_perm_b32 v53, v61, v60, s8
	v_perm_b32 v52, v59, v58, s8
	v_lshl_add_u64 v[58:59], v[50:51], 1, v[56:57]
	global_store_dwordx4 v[58:59], v[52:55], off
	ds_read_u16 v52, v187 offset:4752
	ds_read_u16 v53, v187 offset:5280
	ds_read_u16 v54, v187 offset:7392
	ds_read_u16 v55, v187 offset:7920
	ds_read_u16 v60, v187 offset:5808
	ds_read_u16 v61, v187 offset:6336
	ds_read_u16 v62, v187 offset:8976
	ds_read_u16 v63, v187 offset:6864
	ds_read_u16 v64, v188
	ds_read_u16 v65, v188 offset:4224
	ds_read_u16 v66, v187 offset:9504
	ds_read_u16 v67, v187 offset:10032
	ds_read_u16 v68, v187 offset:10560
	ds_read_u16 v69, v187 offset:11088
	ds_read_u16 v70, v187 offset:11616
	ds_read_u16 v71, v187 offset:12144
	s_waitcnt lgkmcnt(12)
	v_perm_b32 v55, v55, v54, s8
	s_waitcnt lgkmcnt(11)
	v_perm_b32 v53, v60, v53, s8
	s_waitcnt lgkmcnt(7)
	v_perm_b32 v52, v52, v64, s8
	v_perm_b32 v54, v63, v61, s8
	global_store_dwordx4 v[58:59], v[52:55], off offset:16
	v_lshl_add_u64 v[56:57], v[48:49], 1, v[56:57]
	s_waitcnt lgkmcnt(0)
	v_perm_b32 v55, v71, v70, s8
	ds_read_u16 v60, v189
	ds_read_u16 v61, v202
	ds_read_u16 v63, v203
	ds_read_u16 v64, v204
	ds_read_u16 v70, v205
	ds_read_u16 v71, v206
	ds_read_u16 v72, v207
	ds_read_u16 v73, v208
	v_perm_b32 v54, v69, v68, s8
	v_perm_b32 v53, v67, v66, s8
	v_perm_b32 v52, v62, v65, s8
	global_store_dwordx4 v[58:59], v[52:55], off offset:32
	s_waitcnt lgkmcnt(0)
	s_nop 0
	v_perm_b32 v55, v73, v72, s8
	v_perm_b32 v54, v71, v70, s8
	v_perm_b32 v53, v64, v63, s8
	v_perm_b32 v52, v61, v60, s8
	v_readlane_b32 s8, v252, 57
	s_add_i32 s1, s1, s8
	s_cmpk_lt_i32 s0, 0x240
	global_store_dwordx4 v[56:57], v[52:55], off
	s_barrier
	s_cbranch_scc0 .LBB0_271
